# attention work queue: next-ticket returning atomic no longer waited at unit start (returns into the dedicated VGPR; consumed after the unit's closing vmcnt(0))
# baseline (speedup 1.0000x reference)
.LBB0_466:
	v_mov_b32_e32 v194, 0
	s_and_saveexec_b64 s[0:1], s[2:3]
	s_cbranch_execz .LBB0_470
	s_mov_b64 s[44:45], exec
	v_mbcnt_lo_u32_b32 v0, s44, 0
	v_mbcnt_hi_u32_b32 v0, s45, v0
	v_cmp_eq_u32_e32 vcc, 0, v0
	s_and_saveexec_b64 s[6:7], vcc
	s_cbranch_execz .LBB0_469
	s_bcnt1_i32_b64 s8, s[44:45]
	v_mov_b32_e32 v1, s8
	global_atomic_add v194, v117, v1, s[90:91] offset:2048 sc0
.LBB0_469:
	s_or_b64 exec, exec, s[6:7]
.LBB0_470:
	s_or_b64 exec, exec, s[0:1]
	s_lshl_b32 s0, s56, 7
	s_lshr_b32 s33, s56, 8
	s_and_b32 s29, s0, 0x7800
	s_sub_i32 s30, 7, s33
	s_and_b32 s57, s56, 15
	s_mul_i32 s54, s29, 0x1800
	v_readlane_b32 s0, v254, 46
	v_readlane_b32 s1, v254, 47
	s_add_u32 s0, s0, s54
	s_addc_u32 s1, s1, 0
	s_lshl_b32 s55, s57, 7
	s_add_u32 s0, s0, s55
	s_addc_u32 s1, s1, 0
	s_lshl_b32 s6, s30, 8
	v_lshl_add_u64 v[0:1], s[0:1], 0, v[112:113]
	v_lshl_add_u64 v[4:5], s[0:1], 0, v[114:115]
	s_add_i32 s8, s6, s17
	v_lshl_add_u64 v[0:1], v[0:1], 0, s[10:11]
	s_mov_b64 s[6:7], 0x800
	v_lshl_add_u64 v[4:5], v[4:5], 0, s[12:13]
	v_lshl_add_u64 v[2:3], v[0:1], 0, s[6:7]
	v_lshl_add_u64 v[4:5], v[4:5], 0, v[116:117]
	s_mov_b64 s[6:7], 0x1000
	s_mov_b32 m0, s18
	v_lshl_add_u64 v[6:7], v[4:5], 0, s[6:7]
	global_load_lds_dwordx4 v[2:3], off
	s_mov_b32 m0, s20
	s_mov_b64 s[6:7], 0x60800
	global_load_lds_dwordx4 v[6:7], off
	v_lshl_add_u64 v[0:1], v[0:1], 0, s[6:7]
	s_mov_b32 m0, s21
	s_mov_b64 s[6:7], 0x61000
	global_load_lds_dwordx4 v[0:1], off
	v_lshl_add_u64 v[0:1], v[4:5], 0, s[6:7]
	s_mov_b32 m0, s22
	v_or_b32_e32 v195, s8, v161
	global_load_lds_dwordx4 v[0:1], off
	v_mov_b64_e32 v[0:1], s[0:1]
	v_mad_u64_u32 v[0:1], s[0:1], v195, s19, v[0:1]
	s_lshl_b32 s0, s56, 11
	v_lshl_add_u64 v[0:1], v[118:119], 1, v[0:1]
	s_and_b32 s0, s0, 0x7f800
	s_mov_b32 s1, s9
	global_load_dwordx4 v[76:79], v[0:1], off
	global_load_dwordx4 v[72:75], v[0:1], off offset:32
	global_load_dwordx4 v[68:71], v[0:1], off offset:64
	global_load_dwordx4 v[64:67], v[0:1], off offset:96
	v_lshl_add_u64 v[0:1], v[120:121], 0, s[0:1]
	global_load_dword v0, v[0:1], off
	s_cmp_eq_u32 s33, 7
	s_cselect_b64 s[0:1], -1, 0
	v_mov_b32_e32 v16, 0
	s_and_b64 vcc, exec, s[0:1]
	v_mov_b32_e32 v17, 0
	s_waitcnt vmcnt(0)
	v_lshlrev_b32_e32 v26, 16, v76
	v_and_b32_e32 v27, 0xffff0000, v76
	v_lshlrev_b32_e32 v28, 16, v77
	v_and_b32_e32 v29, 0xffff0000, v77
	v_lshlrev_b32_e32 v30, 16, v78
	ds_write_b32 v162, v0
	s_waitcnt vmcnt(0) lgkmcnt(0)
	s_barrier
	v_and_b32_e32 v31, 0xffff0000, v78
	v_lshlrev_b32_e32 v32, 16, v79
	v_and_b32_e32 v33, 0xffff0000, v79
	v_lshlrev_b32_e32 v18, 16, v72
	v_and_b32_e32 v19, 0xffff0000, v72
	v_lshlrev_b32_e32 v20, 16, v73
	v_and_b32_e32 v21, 0xffff0000, v73
	v_lshlrev_b32_e32 v22, 16, v74
	v_and_b32_e32 v23, 0xffff0000, v74
	v_lshlrev_b32_e32 v24, 16, v75
	v_and_b32_e32 v25, 0xffff0000, v75
	v_lshlrev_b32_e32 v15, 16, v68
	v_and_b32_e32 v14, 0xffff0000, v68
	v_lshlrev_b32_e32 v13, 16, v69
	v_and_b32_e32 v12, 0xffff0000, v69
	v_lshlrev_b32_e32 v8, 16, v70
	v_and_b32_e32 v9, 0xffff0000, v70
	v_lshlrev_b32_e32 v10, 16, v71
	v_and_b32_e32 v11, 0xffff0000, v71
	v_lshlrev_b32_e32 v7, 16, v64
	v_and_b32_e32 v6, 0xffff0000, v64
	v_lshlrev_b32_e32 v5, 16, v65
	v_and_b32_e32 v4, 0xffff0000, v65
	v_lshlrev_b32_e32 v3, 16, v66
	v_and_b32_e32 v2, 0xffff0000, v66
	v_lshlrev_b32_e32 v1, 16, v67
	v_and_b32_e32 v0, 0xffff0000, v67
	s_cbranch_vccnz .LBB0_472
	ds_read_b128 v[34:37], v163
	ds_read_b128 v[38:41], v163 offset:16
	s_waitcnt lgkmcnt(0)
	v_fma_f32 v17, v26, v34, 0
	v_fmac_f32_e32 v17, v27, v35
	v_fmac_f32_e32 v17, v28, v36
	v_fmac_f32_e32 v17, v29, v37
	v_fmac_f32_e32 v17, v30, v38
	v_fmac_f32_e32 v17, v31, v39
	v_fmac_f32_e32 v17, v32, v40
	v_fmac_f32_e32 v17, v33, v41
	ds_read_b128 v[34:37], v163 offset:64
	ds_read_b128 v[38:41], v163 offset:80
	s_waitcnt lgkmcnt(1)
	v_fmac_f32_e32 v17, v18, v34
	v_fmac_f32_e32 v17, v19, v35
	v_fmac_f32_e32 v17, v20, v36
	v_fmac_f32_e32 v17, v21, v37
	s_waitcnt lgkmcnt(0)
	v_fmac_f32_e32 v17, v22, v38
	v_fmac_f32_e32 v17, v23, v39
	v_fmac_f32_e32 v17, v24, v40
	v_fmac_f32_e32 v17, v25, v41
	ds_read_b128 v[34:37], v163 offset:128
	ds_read_b128 v[38:41], v163 offset:144
	s_waitcnt lgkmcnt(1)
	v_fmac_f32_e32 v17, v15, v34
	v_fmac_f32_e32 v17, v14, v35
	v_fmac_f32_e32 v17, v13, v36
	v_fmac_f32_e32 v17, v12, v37
	s_waitcnt lgkmcnt(0)
	v_fmac_f32_e32 v17, v8, v38
	v_fmac_f32_e32 v17, v9, v39
	v_fmac_f32_e32 v17, v10, v40
	v_fmac_f32_e32 v17, v11, v41
	ds_read_b128 v[34:37], v163 offset:192
	ds_read_b128 v[38:41], v163 offset:208
	s_waitcnt lgkmcnt(1)
	v_fmac_f32_e32 v17, v7, v34
	v_fmac_f32_e32 v17, v6, v35
	v_fmac_f32_e32 v17, v5, v36
	v_fmac_f32_e32 v17, v4, v37
	s_waitcnt lgkmcnt(0)
	v_fmac_f32_e32 v17, v3, v38
	v_fmac_f32_e32 v17, v2, v39
	v_fmac_f32_e32 v17, v1, v40
	v_fmac_f32_e32 v17, v0, v41
	v_mov_b32_e32 v34, v17
	s_nop 1
	v_permlane32_swap_b32_e32 v17, v34
	v_add_f32_e32 v17, v17, v34

.LBB0_1401:
	v_mov_b32_e32 v188, 0
	s_and_saveexec_b64 s[38:39], s[2:3]
	s_cbranch_execz .LBB0_1405
	s_mov_b64 s[42:43], exec
	v_mbcnt_lo_u32_b32 v0, s42, 0
	v_mbcnt_hi_u32_b32 v0, s43, v0
	v_cmp_eq_u32_e32 vcc, 0, v0
	s_and_saveexec_b64 s[40:41], vcc
	s_cbranch_execz .LBB0_1404
	s_bcnt1_i32_b64 s42, s[42:43]
	v_mov_b32_e32 v1, s42
	global_atomic_add v188, v117, v1, s[90:91] offset:2304 sc0
.LBB0_1404:
	s_or_b64 exec, exec, s[40:41]
.LBB0_1405:
	s_or_b64 exec, exec, s[38:39]
	s_and_b32 s45, s0, 15
	s_lshl_b32 s39, s45, 2
	s_mov_b32 s64, s62
	v_mov_b32_e32 v0, s39
	v_readlane_b32 s48, v254, 6
	s_lshl_b32 s39, s0, 7
	s_lshr_b32 s38, s0, 8
	v_readlane_b32 s49, v254, 7
	s_and_b32 s40, s39, 0x7800
	s_sub_i32 s46, 7, s38
	s_mul_i32 s39, s40, 0xc00
	v_readlane_b32 s48, v254, 46
	v_readlane_b32 s49, v254, 47
	s_add_u32 s43, s48, s39
	s_addc_u32 s44, s49, 0
	s_lshl_b32 s0, s0, 5
	v_readlane_b32 s50, v254, 8
	s_and_b32 s0, s0, 0x180
	v_readlane_b32 s51, v254, 9
	s_add_u32 s50, s43, s0
	s_addc_u32 s51, s44, 0
	s_lshl_b32 s39, s46, 2
	s_or_b32 s0, s39, 3
	s_add_i32 s41, s39, -2
	v_lshl_add_u64 v[2:3], s[50:51], 0, v[112:113]
	s_cmp_lg_u32 s38, 7
	v_lshl_add_u64 v[130:131], v[2:3], 0, s[6:7]
	v_lshl_add_u64 v[2:3], s[50:51], 0, v[114:115]
	s_cselect_b32 s49, s41, 0
	v_lshl_add_u64 v[2:3], v[2:3], 0, s[8:9]
	v_lshl_add_u64 v[132:133], v[2:3], 0, v[116:117]
	v_mad_u64_u32 v[2:3], s[50:51], s49, v184, v[130:131]
	s_mov_b32 m0, s20
	v_lshl_add_u64 v[2:3], v[2:3], 0, s[10:11]
	v_readlane_b32 s60, v254, 18
	v_readlane_b32 s61, v254, 19
	global_load_lds_dwordx4 v[2:3], off
	v_mad_u64_u32 v[2:3], s[50:51], s49, v184, v[132:133]
	v_lshl_add_u64 v[2:3], v[2:3], 0, s[12:13]
	s_nop 1
	global_load_dword v0, v0, s[60:61]
	s_mov_b32 m0, s23
	s_sub_i32 s42, s0, s49
	global_load_lds_dwordx4 v[2:3], off
	s_cmp_lt_i32 s42, 1
	v_readlane_b32 s52, v254, 10
	v_readlane_b32 s53, v254, 11
	v_readlane_b32 s54, v254, 12
	v_readlane_b32 s55, v254, 13
	v_readlane_b32 s56, v254, 14
	v_readlane_b32 s57, v254, 15
	v_readlane_b32 s58, v254, 16
	v_readlane_b32 s59, v254, 17
	v_readlane_b32 s62, v254, 20
	v_readlane_b32 s63, v254, 21
	s_cbranch_scc1 .LBB0_1407
	s_or_b32 s0, s49, 1
	v_mad_u64_u32 v[2:3], s[50:51], s0, v184, v[130:131]
	s_mov_b32 m0, s28
	v_lshl_add_u64 v[2:3], v[2:3], 0, s[10:11]
	global_load_lds_dwordx4 v[2:3], off
	v_mad_u64_u32 v[2:3], s[50:51], s0, v184, v[132:133]
	v_lshl_add_u64 v[2:3], v[2:3], 0, s[12:13]
	s_mov_b32 m0, s29
	s_nop 0
	global_load_lds_dwordx4 v[2:3], off

.LBB0_2278:
	v_mov_b32_e32 v211, 0
	s_and_saveexec_b64 s[8:9], s[2:3]
	s_cbranch_execz .LBB0_2282
	s_mov_b64 s[12:13], exec
	v_mbcnt_lo_u32_b32 v0, s12, 0
	v_mbcnt_hi_u32_b32 v0, s13, v0
	v_cmp_eq_u32_e32 vcc, 0, v0
	s_and_saveexec_b64 s[10:11], vcc
	s_cbranch_execz .LBB0_2281
	s_bcnt1_i32_b64 s12, s[12:13]
	v_mov_b32_e32 v1, s12
	global_atomic_add v211, v157, v1, s[90:91] offset:2560 sc0
.LBB0_2281:
	s_or_b64 exec, exec, s[10:11]
.LBB0_2282:
	s_or_b64 exec, exec, s[8:9]
	s_lshl_b32 s8, s0, 7
	s_lshr_b32 s74, s0, 8
	s_and_b32 s79, s8, 0x7800
	s_sub_i32 s12, 7, s74
	s_mul_i32 s8, s79, 0x1800
	v_readlane_b32 s10, v254, 46
	v_readlane_b32 s11, v254, 47
	s_add_u32 s8, s10, s8
	s_addc_u32 s9, s11, 0
	s_lshl_b32 s0, s0, 6
	s_and_b32 s78, s0, 0x3c0
	s_lshl_b32 s0, s78, 1
	s_add_u32 s8, s8, s0
	s_addc_u32 s9, s9, 0
	s_lshl_b32 s0, s12, 8
	v_readlane_b32 s10, v255, 3
	s_add_i32 s0, s0, s10
	v_readlane_b32 s10, v254, 61
	v_lshl_add_u64 v[2:3], s[8:9], 0, v[152:153]
	v_readlane_b32 s11, v254, 62
	v_lshl_add_u64 v[4:5], s[8:9], 0, v[154:155]
	s_lshl_b32 s86, s12, 2
	v_lshl_add_u64 v[170:171], v[2:3], 0, s[10:11]
	v_readlane_b32 s10, v254, 63
	v_readlane_b32 s11, v255, 0
	s_or_b32 s13, s86, 3
	s_mov_b32 m0, s73
	v_lshl_add_u64 v[4:5], v[4:5], 0, s[10:11]
	v_lshl_add_u64 v[4:5], v[4:5], 0, v[156:157]
	s_mov_b64 s[10:11], 0x1000
	v_lshl_add_u64 v[172:173], v[4:5], 0, s[10:11]
	s_mul_i32 s10, s13, 0x30000
	s_mov_b32 s11, s1
	s_lshl_b64 s[10:11], s[10:11], 1
	v_lshl_add_u64 v[4:5], v[170:171], 0, s[10:11]
	v_lshl_add_u64 v[4:5], v[4:5], 0, s[84:85]
	global_load_lds_dwordx4 v[4:5], off
	v_lshl_add_u64 v[4:5], v[172:173], 0, s[10:11]
	v_readlane_b32 s10, v255, 1
	s_mul_i32 s12, s12, 0xc0000
	s_mov_b32 m0, s10
	s_add_i32 s10, s12, 0x60000
	s_mov_b32 s11, s1
	v_lshl_add_u64 v[2:3], v[170:171], 0, s[84:85]
	s_lshl_b64 s[10:11], s[10:11], 1
	v_readlane_b32 s14, v255, 2
	global_load_lds_dwordx4 v[4:5], off
	v_lshl_add_u64 v[4:5], v[2:3], 0, s[10:11]
	s_mov_b32 m0, s14
	v_or_b32_e32 v0, s0, v174
	global_load_lds_dwordx4 v[4:5], off
	v_lshl_add_u64 v[4:5], v[172:173], 0, s[10:11]
	v_readlane_b32 s10, v255, 6
	s_mov_b32 m0, s10
	v_readlane_b32 s10, v255, 7
	global_load_lds_dwordx4 v[4:5], off
	v_mov_b64_e32 v[4:5], s[8:9]
	s_movk_i32 s8, 0x1800
	v_mad_u64_u32 v[4:5], s[8:9], v0, s8, v[4:5]
	s_or_b32 s8, s12, 0x30000
	s_mov_b32 s9, s1
	v_lshl_add_u64 v[4:5], v[158:159], 1, v[4:5]
	s_lshl_b64 s[8:9], s[8:9], 1
	global_load_dwordx4 v[104:107], v[4:5], off
	global_load_dwordx4 v[108:111], v[4:5], off offset:32
	global_load_dwordx4 v[112:115], v[4:5], off offset:64
	global_load_dwordx4 v[116:119], v[4:5], off offset:96
	s_waitcnt vmcnt(2) lgkmcnt(0)
	s_barrier
	v_lshl_add_u64 v[2:3], v[2:3], 0, s[8:9]
	s_mov_b32 m0, s10
	s_or_b32 s87, s0, 31
	global_load_lds_dwordx4 v[2:3], off
	v_lshl_add_u64 v[2:3], v[172:173], 0, s[8:9]
	v_readlane_b32 s8, v255, 8
	s_mov_b32 m0, s8
	s_lshl_b32 s8, s13, 6
	global_load_lds_dwordx4 v[2:3], off
	s_cmp_ge_u32 s8, s87
	s_cbranch_scc1 .LBB0_2285
	s_cmp_eq_u64 exec, 0
	s_cbranch_scc1 .LBB0_2306
	ds_read_b128 v[2:5], v176
	ds_read_b128 v[18:21], v176 offset:512
	ds_read_b128 v[36:39], v176 offset:2048
	ds_read_b128 v[40:43], v176 offset:2560
	ds_read_b64_tr_b16 v[92:93], v177 offset:24576
	ds_read_b64_tr_b16 v[94:95], v177 offset:25088
	ds_read_b64_tr_b16 v[84:85], v177 offset:25600
	ds_read_b64_tr_b16 v[86:87], v177 offset:26112
	ds_read_b128 v[44:47], v176 offset:4096
	ds_read_b128 v[48:51], v176 offset:4608
	s_waitcnt vmcnt(0) lgkmcnt(0)
	v_mfma_f32_32x32x16_bf16 v[2:17], v[2:5], v[104:107], 0
	ds_read_b64_tr_b16 v[76:77], v177 offset:26624
	ds_read_b64_tr_b16 v[78:79], v177 offset:27136
	ds_read_b64_tr_b16 v[68:69], v177 offset:27648
	ds_read_b64_tr_b16 v[70:71], v177 offset:28160
	ds_read_b128 v[52:55], v176 offset:6144
	ds_read_b128 v[56:59], v176 offset:6656
	v_mfma_f32_32x32x16_bf16 v[20:35], v[18:21], v[104:107], 0
	v_mfma_f32_32x32x16_bf16 v[2:17], v[36:39], v[108:111], v[2:17]
	v_mfma_f32_32x32x16_bf16 v[20:35], v[40:43], v[108:111], v[20:35]
	v_mfma_f32_32x32x16_bf16 v[2:17], v[44:47], v[112:115], v[2:17]
	v_mfma_f32_32x32x16_bf16 v[20:35], v[48:51], v[112:115], v[20:35]
	s_waitcnt lgkmcnt(1)
	v_mfma_f32_32x32x16_bf16 v[2:17], v[52:55], v[116:119], v[2:17]
	ds_read_b64_tr_b16 v[120:121], v177 offset:28672
	ds_read_b64_tr_b16 v[122:123], v177 offset:29184
	ds_read_b64_tr_b16 v[88:89], v177 offset:29696
	ds_read_b64_tr_b16 v[90:91], v177 offset:30208
	s_waitcnt lgkmcnt(4)
	v_mfma_f32_32x32x16_bf16 v[20:35], v[56:59], v[116:119], v[20:35]
	ds_read_b64_tr_b16 v[80:81], v177 offset:30720
	ds_read_b64_tr_b16 v[82:83], v177 offset:31232
	ds_read_b64_tr_b16 v[72:73], v177 offset:31744
	ds_read_b64_tr_b16 v[74:75], v177 offset:32256
	s_nop 7
	v_max_f32_e32 v36, v20, v20
	v_min_f32_e32 v37, 0x42700000, v36
	v_exp_f32_e32 v37, v37
	v_add_u32_e32 v1, s8, v175
	v_max_f32_e32 v18, v2, v2
	v_max_f32_e32 v39, v21, v21
	v_min_f32_e32 v19, 0x42700000, v18
	v_sub_u32_e32 v0, v0, v1
	v_add_f32_e32 v1, 1.0, v37
	v_max_f32_e32 v37, v3, v3
	v_min_f32_e32 v41, 0x42700000, v39
	v_exp_f32_e32 v19, v19
	v_min_f32_e32 v38, 0x42700000, v37
	v_exp_f32_e32 v41, v41
	v_exp_f32_e32 v38, v38
	v_add_f32_e32 v19, 1.0, v19
	v_log_f32_e32 v19, v19
	v_add_f32_e32 v41, 1.0, v41
	v_log_f32_e32 v1, v1
	v_add_f32_e32 v38, 1.0, v38
	v_log_f32_e32 v41, v41
	v_log_f32_e32 v38, v38
	v_max_f32_e32 v43, v22, v22
	v_min_f32_e32 v44, 0x42700000, v43
	v_max_f32_e32 v18, v19, v18
	v_cmp_lt_i32_e32 vcc, 0, v0
	v_max_f32_e32 v1, v1, v36
	v_cmp_lt_i32_e64 s[8:9], 32, v0
	v_max_f32_e32 v129, v41, v39
	v_max_f32_e32 v39, v4, v4
	v_exp_f32_e32 v44, v44
	v_cndmask_b32_e64 v19, 0, -v18, vcc
	v_cndmask_b32_e64 v40, 0, -v1, s[8:9]
	v_max_f32_e32 v128, v38, v37
	v_cmp_lt_i32_e64 s[14:15], 1, v0
	v_cmp_lt_i32_e64 s[10:11], 33, v0
	v_min_f32_e32 v42, 0x42700000, v39
	v_add_f32_e32 v36, v19, v40
	v_cndmask_b32_e64 v37, 0, -v128, s[14:15]
	v_cndmask_b32_e64 v41, 0, -v129, s[10:11]
	v_exp_f32_e32 v42, v42
	v_add_f32_e32 v36, 0, v36
	v_add_f32_e32 v38, v37, v41
	v_add_f32_e32 v36, v38, v36
	v_add_f32_e32 v38, 1.0, v44
	v_log_f32_e32 v38, v38
	v_add_f32_e32 v42, 1.0, v42
	v_log_f32_e32 v42, v42
	v_max_f32_e32 v45, v23, v23
	v_max_f32_e32 v131, v38, v43
	v_max_f32_e32 v43, v5, v5
	v_min_f32_e32 v46, 0x42700000, v45
	v_min_f32_e32 v44, 0x42700000, v43
	v_exp_f32_e32 v46, v46
	v_max_f32_e32 v130, v42, v39
	v_cmp_lt_i32_e64 s[16:17], 2, v0
	v_cmp_lt_i32_e64 s[18:19], 34, v0
	v_exp_f32_e32 v44, v44
	v_cndmask_b32_e64 v39, 0, -v130, s[16:17]
	v_cndmask_b32_e64 v42, 0, -v131, s[18:19]
	v_add_f32_e32 v38, v39, v42
	v_add_f32_e32 v36, v38, v36
	v_add_f32_e32 v38, 1.0, v46
	v_add_f32_e32 v44, 1.0, v44
	v_log_f32_e32 v38, v38
	v_log_f32_e32 v44, v44
	v_max_f32_e32 v47, v24, v24
	v_min_f32_e32 v48, 0x42700000, v47
	v_max_f32_e32 v133, v38, v45
	v_max_f32_e32 v45, v6, v6
	v_exp_f32_e32 v48, v48
	v_max_f32_e32 v132, v44, v43
	v_cmp_lt_i32_e64 s[24:25], 3, v0
	v_cmp_lt_i32_e64 s[20:21], 35, v0
	v_min_f32_e32 v46, 0x42700000, v45
	v_cndmask_b32_e64 v43, 0, -v132, s[24:25]
	v_cndmask_b32_e64 v44, 0, -v133, s[20:21]
	v_exp_f32_e32 v46, v46
	v_add_f32_e32 v38, v43, v44
	v_add_f32_e32 v36, v38, v36
	v_add_f32_e32 v38, 1.0, v48
	v_log_f32_e32 v38, v38
	v_add_f32_e32 v46, 1.0, v46
	v_log_f32_e32 v46, v46
	v_max_f32_e32 v49, v25, v25
	v_max_f32_e32 v135, v38, v47
	v_max_f32_e32 v47, v7, v7
	v_min_f32_e32 v50, 0x42700000, v49
	v_min_f32_e32 v48, 0x42700000, v47
	v_exp_f32_e32 v50, v50
	v_max_f32_e32 v134, v46, v45
	v_cmp_lt_i32_e64 s[26:27], 8, v0
	v_cmp_lt_i32_e64 s[28:29], 40, v0
	v_exp_f32_e32 v48, v48
	v_cndmask_b32_e64 v45, 0, -v134, s[26:27]
	v_cndmask_b32_e64 v46, 0, -v135, s[28:29]
	v_add_f32_e32 v38, v45, v46
	v_add_f32_e32 v36, v38, v36
	v_add_f32_e32 v38, 1.0, v50
	v_add_f32_e32 v48, 1.0, v48
	v_log_f32_e32 v38, v38
	v_log_f32_e32 v48, v48
	v_cmp_lt_i32_e64 s[38:39], 9, v0
	v_cmp_lt_i32_e64 s[34:35], 41, v0
	v_max_f32_e32 v137, v38, v49
	v_max_f32_e32 v38, v8, v8
	v_max_f32_e32 v136, v48, v47
	v_min_f32_e32 v48, 0x42700000, v38
	v_exp_f32_e32 v48, v48
	v_cndmask_b32_e64 v47, 0, -v136, s[38:39]
	v_cndmask_b32_e64 v49, 0, -v137, s[34:35]
	v_add_f32_e32 v50, v47, v49
	v_add_f32_e32 v36, v50, v36
	v_max_f32_e32 v50, v26, v26
	v_add_f32_e32 v48, 1.0, v48
	v_min_f32_e32 v51, 0x42700000, v50
	v_log_f32_e32 v48, v48
	v_exp_f32_e32 v51, v51
	v_cmp_lt_i32_e64 s[40:41], 10, v0
	v_cmp_lt_i32_e64 s[46:47], 42, v0
	v_max_f32_e32 v138, v48, v38
	v_add_f32_e32 v38, 1.0, v51
	v_max_f32_e32 v51, v9, v9
	v_min_f32_e32 v52, 0x42700000, v51
	v_log_f32_e32 v38, v38
	v_exp_f32_e32 v52, v52
	v_cndmask_b32_e64 v48, 0, -v138, s[40:41]
	v_cmp_lt_i32_e64 s[52:53], 11, v0
	v_max_f32_e32 v139, v38, v50
	v_add_f32_e32 v38, 1.0, v52
	v_max_f32_e32 v52, v27, v27
	v_log_f32_e32 v38, v38
	v_min_f32_e32 v53, 0x42700000, v52
	v_exp_f32_e32 v53, v53
	v_cndmask_b32_e64 v50, 0, -v139, s[46:47]
	v_add_f32_e32 v54, v48, v50
	v_max_f32_e32 v141, v38, v51
	v_max_f32_e32 v38, v10, v10
	v_add_f32_e32 v140, v54, v36
	v_add_f32_e32 v36, 1.0, v53
	v_min_f32_e32 v51, 0x42700000, v38
	v_log_f32_e32 v36, v36
	v_exp_f32_e32 v51, v51
	v_cndmask_b32_e64 v53, 0, -v141, s[52:53]
	v_cmp_lt_i32_e64 s[48:49], 43, v0
	v_max_f32_e32 v142, v36, v52
	v_add_f32_e32 v36, 1.0, v51
	v_max_f32_e32 v51, v28, v28
	v_log_f32_e32 v36, v36
	v_min_f32_e32 v52, 0x42700000, v51
	v_exp_f32_e32 v52, v52
	v_cndmask_b32_e64 v124, 0, -v142, s[48:49]
	v_max_f32_e32 v144, v36, v38
	v_max_f32_e32 v38, v11, v11
	v_add_f32_e32 v36, 1.0, v52
	v_min_f32_e32 v52, 0x42700000, v38
	v_log_f32_e32 v36, v36
	v_exp_f32_e32 v52, v52
	v_add_f32_e32 v143, v53, v124
	v_cmp_lt_i32_e64 s[54:55], 16, v0
	v_max_f32_e32 v146, v36, v51
	v_add_f32_e32 v36, 1.0, v52
	v_max_f32_e32 v51, v29, v29
	v_log_f32_e32 v36, v36
	v_min_f32_e32 v52, 0x42700000, v51
	v_exp_f32_e32 v52, v52
	v_cmp_lt_i32_e64 s[60:61], 17, v0
	v_max_f32_e32 v148, v36, v38
	v_max_f32_e32 v38, v12, v12
	v_add_f32_e32 v36, 1.0, v52
	v_min_f32_e32 v52, 0x42700000, v38
	v_log_f32_e32 v36, v36
	v_exp_f32_e32 v52, v52
	v_cmp_lt_i32_e64 s[62:63], 18, v0
	v_cmp_lt_i32_e64 s[66:67], 19, v0
	v_max_f32_e32 v150, v36, v51
	v_add_f32_e32 v36, 1.0, v52
	v_max_f32_e32 v51, v30, v30
	v_log_f32_e32 v36, v36
	v_min_f32_e32 v52, 0x42700000, v51
	v_exp_f32_e32 v52, v52
	v_cmp_lt_i32_e64 s[68:69], 24, v0
	v_max_f32_e32 v212, v36, v38
	v_max_f32_e32 v38, v13, v13
	v_add_f32_e32 v36, 1.0, v52
	v_min_f32_e32 v52, 0x42700000, v38
	v_log_f32_e32 v36, v36
	v_exp_f32_e32 v52, v52
	v_cmp_lt_i32_e64 s[50:51], 25, v0
	v_cmp_lt_i32_e64 s[58:59], 26, v0
	v_max_f32_e32 v214, v36, v51
	v_add_f32_e32 v36, 1.0, v52
	v_max_f32_e32 v51, v31, v31
	v_log_f32_e32 v36, v36
	v_min_f32_e32 v52, 0x42700000, v51
	v_exp_f32_e32 v52, v52
	v_cmp_lt_i32_e64 s[70:71], 27, v0
	v_max_f32_e32 v216, v36, v38
	v_max_f32_e32 v38, v14, v14
	v_add_f32_e32 v36, 1.0, v52
	v_min_f32_e32 v52, 0x42700000, v38
	v_log_f32_e32 v36, v36
	v_exp_f32_e32 v52, v52
	v_cndmask_b32_e64 v145, 0, -v144, s[54:55]
	v_cndmask_b32_e64 v149, 0, -v148, s[60:61]
	v_max_f32_e32 v218, v36, v51
	v_add_f32_e32 v36, 1.0, v52
	v_max_f32_e32 v51, v32, v32
	v_log_f32_e32 v36, v36
	v_min_f32_e32 v52, 0x42700000, v51
	v_exp_f32_e32 v52, v52
	v_cndmask_b32_e64 v213, 0, -v212, s[62:63]
	v_max_f32_e32 v220, v36, v38
	v_max_f32_e32 v38, v15, v15
	v_add_f32_e32 v36, 1.0, v52
	v_min_f32_e32 v52, 0x42700000, v38
	v_log_f32_e32 v36, v36
	v_exp_f32_e32 v52, v52
	v_cndmask_b32_e64 v217, 0, -v216, s[66:67]
	v_cndmask_b32_e64 v221, 0, -v220, s[68:69]
	v_max_f32_e32 v222, v36, v51
	v_add_f32_e32 v36, 1.0, v52
	v_max_f32_e32 v51, v33, v33
	v_log_f32_e32 v36, v36
	v_min_f32_e32 v52, 0x42700000, v51
	v_exp_f32_e32 v52, v52
	s_mov_b32 s81, s80
	v_max_f32_e32 v224, v36, v38
	v_max_f32_e32 v38, v16, v16
	v_add_f32_e32 v36, 1.0, v52
	v_min_f32_e32 v52, 0x42700000, v38
	v_log_f32_e32 v36, v36
	v_exp_f32_e32 v52, v52
	v_cndmask_b32_e64 v225, 0, -v224, s[50:51]
	s_mov_b32 s82, s80
	v_max_f32_e32 v226, v36, v51
	v_add_f32_e32 v36, 1.0, v52
	v_max_f32_e32 v51, v34, v34
	v_log_f32_e32 v36, v36
	v_min_f32_e32 v52, 0x42700000, v51
	v_exp_f32_e32 v52, v52
	s_mov_b32 s83, s80
	v_max_f32_e32 v228, v36, v38
	v_max_f32_e32 v38, v17, v17
	v_add_f32_e32 v36, 1.0, v52
	v_min_f32_e32 v52, 0x42700000, v38
	v_exp_f32_e32 v52, v52
	v_log_f32_e32 v36, v36
	v_cndmask_b32_e64 v229, 0, -v228, s[58:59]
	v_cvt_pk_f16_f32 v40, v40, v41
	v_add_f32_e32 v52, 1.0, v52
	v_log_f32_e32 v52, v52
	v_max_f32_e32 v230, v36, v51
	v_max_f32_e32 v51, v35, v35
	v_min_f32_e32 v36, 0x42700000, v51
	v_max_f32_e32 v232, v52, v38
	v_exp_f32_e32 v125, v36
	v_cvt_pk_f16_f32 v36, v19, v37
	v_cvt_pk_f16_f32 v37, v39, v43
	v_cvt_pk_f16_f32 v38, v45, v47
	v_cvt_pk_f16_f32 v39, v48, v53
	v_cndmask_b32_e64 v233, 0, -v232, s[70:71]
	v_cvt_pk_f16_f32 v41, v42, v44
	v_mfma_f32_32x32x16_f16 v[52:67], v[96:99], v[36:39], 0
	v_cvt_pk_f16_f32 v36, v145, v149
	v_cvt_pk_f16_f32 v37, v213, v217
	v_cvt_pk_f16_f32 v38, v221, v225
	v_cvt_pk_f16_f32 v39, v229, v233
	v_cvt_pk_f16_f32 v42, v46, v49
	v_cvt_pk_f16_f32 v43, v50, v124
	v_add_f32_e32 v19, 1.0, v125
	v_mfma_f32_32x32x16_f16 v[52:67], v[100:103], v[36:39], v[52:67]
	v_mov_b64_e32 v[36:37], s[80:81]
	v_mov_b64_e32 v[38:39], s[82:83]
	v_log_f32_e32 v19, v19
	v_cmp_lt_i32_e64 s[56:57], 48, v0
	v_cmp_lt_i32_e64 s[12:13], 49, v0
	v_cmp_lt_i32_e64 s[22:23], 50, v0
	v_cmp_lt_i32_e64 s[30:31], 51, v0
	v_mfma_f32_32x32x16_f16 v[52:67], v[36:39], v[40:43], v[52:67]
	v_cmp_lt_i32_e64 s[42:43], 56, v0
	v_cmp_lt_i32_e64 s[36:37], 57, v0
	v_cmp_lt_i32_e64 s[44:45], 58, v0
	v_max_f32_e32 v234, v19, v51
	v_cmp_lt_i32_e64 s[64:65], 59, v0
	v_cndmask_b32_e64 v147, 0, -v146, s[56:57]
	v_cndmask_b32_e64 v151, 0, -v150, s[12:13]
	v_cndmask_b32_e64 v215, 0, -v214, s[22:23]
	v_cndmask_b32_e64 v219, 0, -v218, s[30:31]
	v_cndmask_b32_e64 v223, 0, -v222, s[42:43]
	v_cndmask_b32_e64 v227, 0, -v226, s[36:37]
	v_cndmask_b32_e64 v231, 0, -v230, s[44:45]
	v_cndmask_b32_e64 v235, 0, -v234, s[64:65]
	v_cvt_pk_f16_f32 v124, v147, v151
	v_cvt_pk_f16_f32 v125, v215, v219
	v_cvt_pk_f16_f32 v126, v223, v227
	v_cvt_pk_f16_f32 v127, v231, v235
	v_sub_f32_e32 v2, v2, v18
	v_add_f32_e32 v0, v143, v140
	v_mfma_f32_32x32x16_f16 v[52:67], v[36:39], v[124:127], v[52:67]
	v_add_f32_e32 v19, v145, v147
	v_sub_f32_e32 v1, v20, v1
	v_add_f32_e32 v0, v19, v0
	v_add_f32_e32 v19, v149, v151
	v_sub_f32_e32 v3, v3, v128
	v_add_f32_e32 v0, v19, v0
	v_add_f32_e32 v19, v213, v215
	v_mfma_f32_32x32x16_f16 v[36:51], v[96:99], v[40:43], 0
	s_nop 3
	v_add_f32_e32 v18, 0, v52
	v_add_f32_e32 v2, v2, v18
	v_add_f32_e32 v0, v19, v0
	v_add_f32_e32 v19, v217, v219
	v_exp_f32_e32 v2, v2
	v_add_f32_e32 v0, v19, v0
	v_add_f32_e32 v19, v221, v223
	v_mfma_f32_32x32x16_f16 v[36:51], v[100:103], v[124:127], v[36:51]
	v_add_f32_e32 v0, v19, v0
	v_add_f32_e32 v19, v225, v227
	v_add_f32_e32 v0, v19, v0
	v_add_f32_e32 v19, v229, v231
	v_add_f32_e32 v52, v19, v0
	v_cndmask_b32_e32 v0, 0, v2, vcc
	v_sub_f32_e32 v2, v21, v129
	s_nop 4
	v_add_f32_e32 v18, 0, v36
	v_add_f32_e32 v1, v1, v18
	v_add_f32_e32 v18, 0, v53
	v_add_f32_e32 v3, v3, v18
	v_exp_f32_e32 v1, v1
	v_exp_f32_e32 v3, v3
	v_add_f32_e32 v18, 0, v38
	v_sub_f32_e32 v5, v5, v132
	v_cndmask_b32_e64 v53, 0, v1, s[8:9]
	v_cndmask_b32_e64 v1, 0, v3, s[14:15]
	v_add_f32_e32 v3, 0, v37
	v_add_f32_e32 v2, v2, v3
	v_sub_f32_e32 v3, v4, v130
	v_add_f32_e32 v4, 0, v54
	v_add_f32_e32 v3, v3, v4
	v_sub_f32_e32 v4, v22, v131
	v_add_f32_e32 v4, v4, v18
	v_add_f32_e32 v18, 0, v55
	v_add_f32_e32 v5, v5, v18
	v_exp_f32_e32 v2, v2
	v_exp_f32_e32 v3, v3
	v_exp_f32_e32 v4, v4
	v_exp_f32_e32 v5, v5
	v_cndmask_b32_e64 v54, 0, v2, s[10:11]
	v_cndmask_b32_e64 v2, 0, v3, s[16:17]
	v_cndmask_b32_e64 v55, 0, v4, s[18:19]
	v_cndmask_b32_e64 v3, 0, v5, s[24:25]
	v_sub_f32_e32 v4, v23, v133
	v_add_f32_e32 v5, 0, v39
	v_add_f32_e32 v4, v4, v5
	v_sub_f32_e32 v5, v6, v134
	v_add_f32_e32 v6, 0, v56
	v_add_f32_e32 v5, v5, v6
	v_sub_f32_e32 v6, v24, v135
	v_add_f32_e32 v18, 0, v40
	v_add_f32_e32 v6, v6, v18
	v_sub_f32_e32 v7, v7, v136
	v_add_f32_e32 v18, 0, v57
	v_add_f32_e32 v7, v7, v18
	v_exp_f32_e32 v4, v4
	v_exp_f32_e32 v5, v5
	v_exp_f32_e32 v6, v6
	v_exp_f32_e32 v7, v7
	v_cndmask_b32_e64 v40, 0, v4, s[20:21]
	v_cndmask_b32_e64 v4, 0, v5, s[26:27]
	v_cndmask_b32_e64 v56, 0, v6, s[28:29]
	v_cndmask_b32_e64 v5, 0, v7, s[38:39]
	v_sub_f32_e32 v6, v25, v137
	v_add_f32_e32 v7, 0, v41
	v_add_f32_e32 v6, v6, v7
	v_sub_f32_e32 v7, v8, v138
	v_add_f32_e32 v8, 0, v58
	v_add_f32_e32 v7, v7, v8
	v_sub_f32_e32 v8, v26, v139
	v_add_f32_e32 v18, 0, v42
	v_add_f32_e32 v8, v8, v18
	v_sub_f32_e32 v9, v9, v141
	v_add_f32_e32 v18, 0, v59
	v_add_f32_e32 v9, v9, v18
	v_exp_f32_e32 v6, v6
	v_exp_f32_e32 v7, v7
	v_exp_f32_e32 v8, v8
	v_exp_f32_e32 v9, v9
	v_cndmask_b32_e64 v41, 0, v6, s[34:35]
	v_cndmask_b32_e64 v6, 0, v7, s[40:41]
	v_cndmask_b32_e64 v42, 0, v8, s[46:47]
	v_cndmask_b32_e64 v7, 0, v9, s[52:53]
	v_sub_f32_e32 v8, v27, v142
	v_add_f32_e32 v9, 0, v43
	v_add_f32_e32 v8, v8, v9
	v_sub_f32_e32 v9, v10, v144
	v_add_f32_e32 v10, 0, v60
	v_add_f32_e32 v9, v9, v10
	v_sub_f32_e32 v10, v28, v146
	v_add_f32_e32 v18, 0, v44
	v_add_f32_e32 v10, v10, v18
	v_exp_f32_e32 v9, v9
	v_exp_f32_e32 v10, v10
	v_exp_f32_e32 v8, v8
	v_sub_f32_e32 v11, v11, v148
	v_cndmask_b32_e64 v36, 0, v9, s[54:55]
	v_cndmask_b32_e64 v44, 0, v10, s[56:57]
	v_sub_f32_e32 v9, v12, v212
	v_add_f32_e32 v10, 0, v62
	v_add_f32_e32 v9, v9, v10
	v_exp_f32_e32 v9, v9
	v_cndmask_b32_e64 v43, 0, v8, s[48:49]
	v_sub_f32_e32 v8, v29, v150
	v_add_f32_e32 v10, 0, v45
	v_add_f32_e32 v8, v8, v10
	v_cndmask_b32_e64 v38, 0, v9, s[62:63]
	v_sub_f32_e32 v9, v13, v216
	v_add_f32_e32 v10, 0, v63
	v_add_f32_e32 v9, v9, v10
	v_exp_f32_e32 v9, v9
	v_exp_f32_e32 v45, v8
	v_sub_f32_e32 v8, v30, v214
	v_add_f32_e32 v10, 0, v46
	v_add_f32_e32 v8, v8, v10
	v_cndmask_b32_e64 v39, 0, v9, s[66:67]
	v_sub_f32_e32 v9, v14, v220
	v_add_f32_e32 v10, 0, v64
	v_add_f32_e32 v9, v9, v10
	v_exp_f32_e32 v9, v9
	v_add_f32_e32 v18, 0, v61
	v_add_f32_e32 v11, v11, v18
	v_exp_f32_e32 v46, v8
	v_sub_f32_e32 v8, v31, v218
	v_add_f32_e32 v10, 0, v47
	v_exp_f32_e32 v11, v11
	v_add_f32_e32 v8, v8, v10
	v_sub_f32_e32 v16, v16, v228
	v_add_f32_e32 v22, 0, v66
	v_exp_f32_e32 v47, v8
	v_cndmask_b32_e64 v57, 0, v9, s[68:69]
	v_sub_f32_e32 v8, v32, v222
	v_add_f32_e32 v9, 0, v48
	v_add_f32_e32 v16, v16, v22
	v_add_f32_e32 v32, v8, v9
	v_sub_f32_e32 v8, v15, v224
	v_add_f32_e32 v9, 0, v65
	v_exp_f32_e32 v58, v16
	v_sub_f32_e32 v16, v17, v232
	v_add_f32_e32 v17, 0, v67
	v_add_f32_e32 v8, v8, v9
	v_cvt_pk_bf16_f32 v18, v0, v1
	v_cvt_pk_bf16_f32 v19, v2, v3
	v_cvt_pk_bf16_f32 v20, v4, v5
	v_cvt_pk_bf16_f32 v21, v6, v7
	v_add_f32_e32 v16, v16, v17
	v_cndmask_b32_e64 v37, 0, v11, s[60:61]
	v_exp_f32_e32 v48, v8
	v_mfma_f32_32x32x16_bf16 v[0:15], v[18:21], v[92:95], 0
	v_exp_f32_e32 v59, v16
	v_cndmask_b32_e64 v58, 0, v58, s[58:59]
	v_cndmask_b32_e64 v48, 0, v48, s[50:51]
	v_cvt_pk_bf16_f32 v36, v36, v37
	v_cndmask_b32_e64 v59, 0, v59, s[70:71]
	v_cvt_pk_bf16_f32 v37, v38, v39
	v_cvt_pk_bf16_f32 v38, v57, v48
	s_waitcnt lgkmcnt(6)
	v_mfma_f32_32x32x16_bf16 v[16:31], v[18:21], v[120:123], 0
	v_cvt_pk_bf16_f32 v39, v58, v59
	v_exp_f32_e32 v32, v32
	v_cndmask_b32_e64 v45, 0, v45, s[12:13]
	v_cndmask_b32_e64 v46, 0, v46, s[22:23]
	v_cndmask_b32_e64 v47, 0, v47, s[30:31]
	v_cndmask_b32_e64 v48, 0, v32, s[42:43]
	v_sub_f32_e32 v32, v33, v226
	v_mfma_f32_32x32x16_bf16 v[0:15], v[36:39], v[84:87], v[0:15]
	v_add_f32_e32 v33, 0, v49
	v_add_f32_e32 v32, v32, v33
	v_sub_f32_e32 v33, v34, v230
	v_add_f32_e32 v34, 0, v50
	v_add_f32_e32 v33, v33, v34
	v_sub_f32_e32 v34, v35, v234
	v_add_f32_e32 v35, 0, v51
	s_waitcnt lgkmcnt(4)
	v_mfma_f32_32x32x16_bf16 v[16:31], v[36:39], v[88:91], v[16:31]
	v_cvt_pk_bf16_f32 v36, v53, v54
	v_cvt_pk_bf16_f32 v37, v55, v40
	v_cvt_pk_bf16_f32 v38, v56, v41
	v_cvt_pk_bf16_f32 v39, v42, v43
	v_exp_f32_e32 v32, v32
	v_add_f32_e32 v34, v34, v35
	v_exp_f32_e32 v33, v33
	v_mfma_f32_32x32x16_bf16 v[0:15], v[36:39], v[76:79], v[0:15]
	v_exp_f32_e32 v34, v34
	v_cndmask_b32_e64 v35, 0, v32, s[36:37]
	v_cvt_pk_bf16_f32 v32, v44, v45
	v_readlane_b32 s62, v254, 59
	v_readlane_b32 s63, v254, 60
	s_waitcnt lgkmcnt(2)
	v_mfma_f32_32x32x16_bf16 v[16:31], v[36:39], v[80:83], v[16:31]
	v_cndmask_b32_e64 v36, 0, v33, s[44:45]
	v_cndmask_b32_e64 v37, 0, v34, s[64:65]
	v_cvt_pk_bf16_f32 v33, v46, v47
	v_cvt_pk_bf16_f32 v34, v48, v35
	v_cvt_pk_bf16_f32 v35, v36, v37
	v_add_f32_e32 v36, v233, v235
	v_add_f32_e32 v36, v36, v52
	v_mfma_f32_32x32x16_bf16 v[0:15], v[32:35], v[68:71], v[0:15]
	v_mov_b32_e32 v37, v36
	s_nop 1
	v_permlane32_swap_b32_e32 v36, v37
	v_add_f32_e32 v36, v36, v37
	v_add_f32_e32 v212, 0, v36
	s_waitcnt lgkmcnt(0)
	v_mfma_f32_32x32x16_bf16 v[16:31], v[32:35], v[72:75], v[16:31]
	s_mov_b64 s[10:11], exec
	v_cmp_gt_f32_e32 vcc, s72, v212
	s_and_saveexec_b64 s[8:9], s[4:5]
	s_cbranch_execnz .LBB0_2286
	s_branch .LBB0_2287

.LBB0_3005:
	v_mov_b32_e32 v194, 0
	s_and_saveexec_b64 s[0:1], s[2:3]
	s_cbranch_execz .LBB0_3009
	s_mov_b64 s[30:31], exec
	v_mbcnt_lo_u32_b32 v0, s30, 0
	v_mbcnt_hi_u32_b32 v0, s31, v0
	v_cmp_eq_u32_e32 vcc, 0, v0
	s_and_saveexec_b64 s[6:7], vcc
	s_cbranch_execz .LBB0_3008
	s_bcnt1_i32_b64 s8, s[30:31]
	v_mov_b32_e32 v1, s8
	global_atomic_add v194, v117, v1, s[90:91] offset:2816 sc0
.LBB0_3008:
	s_or_b64 exec, exec, s[6:7]
.LBB0_3009:
	s_or_b64 exec, exec, s[0:1]
	s_lshl_b32 s0, s56, 7
	s_lshr_b32 s53, s56, 8
	s_and_b32 s50, s0, 0x7800
	s_sub_i32 s52, 7, s53
	s_and_b32 s57, s56, 15
	s_mul_i32 s54, s50, 0x1800
	v_readlane_b32 s0, v254, 46
	v_readlane_b32 s1, v254, 47
	s_add_u32 s0, s0, s54
	s_addc_u32 s1, s1, 0
	s_lshl_b32 s55, s57, 7
	s_add_u32 s0, s0, s55
	s_addc_u32 s1, s1, 0
	s_lshl_b32 s6, s52, 8
	s_add_i32 s8, s6, s42
	s_lshl_b32 s6, s56, 11
	s_and_b32 s6, s6, 0x7f800
	s_mov_b32 s7, s9
	v_lshl_add_u64 v[2:3], v[120:121], 0, s[6:7]
	global_load_dword v10, v[2:3], off
	v_lshl_add_u64 v[2:3], s[0:1], 0, v[112:113]
	v_or_b32_e32 v195, s8, v161
	v_mov_b64_e32 v[0:1], s[0:1]
	v_lshl_add_u64 v[4:5], s[0:1], 0, v[114:115]
	v_lshl_add_u64 v[2:3], v[2:3], 0, s[10:11]
	s_mov_b64 s[0:1], 0x800
	v_mad_u64_u32 v[0:1], s[6:7], v195, s44, v[0:1]
	v_lshl_add_u64 v[4:5], v[4:5], 0, s[12:13]
	v_lshl_add_u64 v[6:7], v[2:3], 0, s[0:1]
	s_mov_b64 s[0:1], 0x60800
	s_mov_b32 m0, s43
	v_lshl_add_u64 v[0:1], v[118:119], 1, v[0:1]
	v_lshl_add_u64 v[4:5], v[4:5], 0, v[116:117]
	v_lshl_add_u64 v[2:3], v[2:3], 0, s[0:1]
	s_mov_b64 s[0:1], 0x1000
	global_load_dwordx4 v[76:79], v[0:1], off
	global_load_dwordx4 v[72:75], v[0:1], off offset:32
	v_lshl_add_u64 v[8:9], v[4:5], 0, s[0:1]
	global_load_lds_dwordx4 v[6:7], off
	s_mov_b32 m0, s45
	global_load_dwordx4 v[68:71], v[0:1], off offset:64
	global_load_dwordx4 v[64:67], v[0:1], off offset:96
	s_mov_b64 s[0:1], 0x61000
	global_load_lds_dwordx4 v[8:9], off
	s_mov_b32 m0, s46
	v_lshl_add_u64 v[0:1], v[4:5], 0, s[0:1]
	global_load_lds_dwordx4 v[2:3], off
	s_mov_b32 m0, s47
	s_cmp_eq_u32 s53, 7
	global_load_lds_dwordx4 v[0:1], off
	s_cselect_b64 s[0:1], -1, 0
	v_mov_b32_e32 v0, 0
	s_and_b64 vcc, exec, s[0:1]
	v_mov_b32_e32 v1, 0
	s_waitcnt vmcnt(0)
	ds_write_b32 v162, v10
	s_waitcnt vmcnt(0) lgkmcnt(0)
	s_barrier
	v_lshlrev_b32_e32 v28, 16, v76
	v_and_b32_e32 v29, 0xffff0000, v76
	v_lshlrev_b32_e32 v30, 16, v77
	v_and_b32_e32 v31, 0xffff0000, v77
	v_lshlrev_b32_e32 v32, 16, v78
	v_and_b32_e32 v33, 0xffff0000, v78
	v_lshlrev_b32_e32 v34, 16, v79
	v_and_b32_e32 v35, 0xffff0000, v79
	v_lshlrev_b32_e32 v18, 16, v72
	v_and_b32_e32 v19, 0xffff0000, v72
	v_lshlrev_b32_e32 v20, 16, v73
	v_and_b32_e32 v21, 0xffff0000, v73
	v_lshlrev_b32_e32 v22, 16, v74
	v_and_b32_e32 v23, 0xffff0000, v74
	v_lshlrev_b32_e32 v24, 16, v75
	v_and_b32_e32 v25, 0xffff0000, v75
	v_lshlrev_b32_e32 v17, 16, v68
	v_and_b32_e32 v16, 0xffff0000, v68
	v_lshlrev_b32_e32 v15, 16, v69
	v_and_b32_e32 v14, 0xffff0000, v69
	v_lshlrev_b32_e32 v10, 16, v70
	v_and_b32_e32 v11, 0xffff0000, v70
	v_lshlrev_b32_e32 v12, 16, v71
	v_and_b32_e32 v13, 0xffff0000, v71
	v_lshlrev_b32_e32 v9, 16, v64
	v_and_b32_e32 v8, 0xffff0000, v64
	v_lshlrev_b32_e32 v7, 16, v65
	v_and_b32_e32 v6, 0xffff0000, v65
	v_lshlrev_b32_e32 v5, 16, v66
	v_and_b32_e32 v4, 0xffff0000, v66
	v_lshlrev_b32_e32 v3, 16, v67
	v_and_b32_e32 v2, 0xffff0000, v67
	s_cbranch_vccnz .LBB0_3011
	ds_read_b128 v[36:39], v163
	ds_read_b128 v[40:43], v163 offset:16
	ds_read_b128 v[44:47], v163 offset:64
	ds_read_b128 v[48:51], v163 offset:80
	ds_read_b128 v[52:55], v163 offset:128
	s_waitcnt lgkmcnt(0)
	v_fma_f32 v1, v28, v36, 0
	v_fmac_f32_e32 v1, v29, v37
	v_fmac_f32_e32 v1, v30, v38
	v_fmac_f32_e32 v1, v31, v39
	v_fmac_f32_e32 v1, v32, v40
	v_fmac_f32_e32 v1, v33, v41
	v_fmac_f32_e32 v1, v34, v42
	v_fmac_f32_e32 v1, v35, v43
	v_fmac_f32_e32 v1, v18, v44
	v_fmac_f32_e32 v1, v19, v45
	v_fmac_f32_e32 v1, v20, v46
	v_fmac_f32_e32 v1, v21, v47
	v_fmac_f32_e32 v1, v22, v48
	v_fmac_f32_e32 v1, v23, v49
	v_fmac_f32_e32 v1, v24, v50
	v_fmac_f32_e32 v1, v25, v51
	ds_read_b128 v[36:39], v163 offset:144
	ds_read_b128 v[40:43], v163 offset:192
	v_fmac_f32_e32 v1, v17, v52
	v_fmac_f32_e32 v1, v16, v53
	v_fmac_f32_e32 v1, v15, v54
	v_fmac_f32_e32 v1, v14, v55
	s_waitcnt lgkmcnt(1)
	v_fmac_f32_e32 v1, v10, v36
	v_fmac_f32_e32 v1, v11, v37
	v_fmac_f32_e32 v1, v12, v38
	v_fmac_f32_e32 v1, v13, v39
	ds_read_b128 v[36:39], v163 offset:208
	s_waitcnt lgkmcnt(1)
	v_fmac_f32_e32 v1, v9, v40
	v_fmac_f32_e32 v1, v8, v41
	v_fmac_f32_e32 v1, v7, v42
	v_fmac_f32_e32 v1, v6, v43
	s_waitcnt lgkmcnt(0)
	v_fmac_f32_e32 v1, v5, v36
	v_fmac_f32_e32 v1, v4, v37
	v_fmac_f32_e32 v1, v3, v38
	v_fmac_f32_e32 v1, v2, v39
	v_mov_b32_e32 v26, v1
	s_nop 1
	v_permlane32_swap_b32_e32 v1, v26
	v_add_f32_e32 v1, v1, v26
